# MoBA attention tile loop: counted vmcnt waits (7..4) when parking tile t+1 K/V in LDS so the t+2 prefetch stays in flight; on top of GLA counted waits
# speedup vs baseline: 1.0004x; 1.0004x over previous
.LBB0_730:
	s_add_i32 s4, s33, 1
	s_cmp_lt_i32 s4, s36
	s_cselect_b64 s[0:1], -1, 0
	s_cmp_ge_i32 s4, s36
	s_cbranch_scc1 .LBB0_732
	s_and_b64 vcc, exec, s[28:29]
	s_cbranch_vccnz .Lmy_att_strict_0
	s_waitcnt vmcnt(7)
	ds_write_b128 v65, v[130:133] offset:21504
	s_waitcnt vmcnt(6)
	ds_write_b128 v172, v[134:137] offset:59392
	s_waitcnt vmcnt(5)
	ds_write_b128 v173, v[138:141] offset:21504
	s_waitcnt vmcnt(4)
	ds_write_b128 v174, v[142:145] offset:59392
	s_branch .LBB0_732
.Lmy_att_strict_0:
	s_waitcnt vmcnt(3)
	ds_write_b128 v65, v[130:133] offset:21504
	s_waitcnt vmcnt(2)
	ds_write_b128 v172, v[134:137] offset:59392
	s_waitcnt vmcnt(1)
	ds_write_b128 v173, v[138:141] offset:21504
	s_waitcnt vmcnt(0)
	ds_write_b128 v174, v[142:145] offset:59392

.LBB0_746:
	s_waitcnt vmcnt(7)
	ds_write_b128 v65, v[150:153] offset:4096
	s_waitcnt vmcnt(6)
	ds_write_b128 v172, v[146:149] offset:38912
	s_waitcnt vmcnt(5)
	ds_write_b128 v173, v[158:161] offset:4096
	s_waitcnt vmcnt(4)
	ds_write_b128 v174, v[154:157] offset:38912

.LBB0_1802:
	s_add_i32 s4, s69, 1
	s_cmp_lt_i32 s4, s33
	s_cselect_b64 s[0:1], -1, 0
	s_cmp_ge_i32 s4, s33
	s_cbranch_scc1 .LBB0_1804
	s_and_b64 vcc, exec, s[2:3]
	s_cbranch_vccnz .Lmy_att_strict_2
	s_waitcnt vmcnt(7)
	ds_write_b128 v65, v[130:133] offset:21504
	s_waitcnt vmcnt(6)
	ds_write_b128 v172, v[134:137] offset:59392
	s_waitcnt vmcnt(5)
	ds_write_b128 v173, v[138:141] offset:21504
	s_waitcnt vmcnt(4)
	ds_write_b128 v174, v[142:145] offset:59392
	s_branch .LBB0_1804
